# hand-written diff-attention epilogue: products as 64 packed v_pk_mul_f32 (row pairs), DPP/pack pairs issued four at a time with rotating temporaries
# baseline (speedup 1.0000x reference)
.Lmk_b1e:
	s_waitcnt vmcnt(8)
	s_waitcnt vmcnt(9)
	ds_write_b128 v0, v[194:197]
	s_waitcnt vmcnt(8)
	ds_write_b128 v0, v[198:201] offset:8192
	s_and_saveexec_b64 s[2:3], s[0:1]
	v_add_f32_e32 v0, v222, v223
	v_fmac_f32_e32 v0, v214, v221
	v_add_f32_e32 v158, v216, v217
	v_fmac_f32_e32 v158, v0, v215
	ds_write_b32 v212, v158
	s_or_b64 exec, exec, s[2:3]
	s_waitcnt lgkmcnt(0)
	ds_read_b128 v[190:193], v211
	s_ashr_i32 s65, s64, 31
	ds_read_b128 v[186:189], v211 offset:32
	ds_read_b128 v[182:185], v211 offset:64
	ds_read_b128 v[158:161], v211 offset:96
	s_lshl_b64 s[0:1], s[64:65], 13
	v_readlane_b32 s2, v254, 17
	s_waitcnt lgkmcnt(3)
	v_rcp_f32_e32 v190, v190
	v_readlane_b32 s3, v254, 18
	s_add_u32 s2, s2, s0
	v_and_b32_e32 v0, 1, v233
	s_addc_u32 s3, s3, s1
	v_cmp_eq_u32_e64 s[0:1], 0, v0
	v_lshlrev_b32_e32 v0, 1, v242
	v_lshl_add_u64 v[194:195], s[2:3], 0, v[0:1]
	v_lshlrev_b32_e32 v0, 15, v210
	v_lshl_add_u64 v[194:195], v[194:195], 0, v[0:1]
	s_waitcnt lgkmcnt(0)
	v_rcp_f32_e32 v191, v191
	v_rcp_f32_e32 v192, v192
	v_rcp_f32_e32 v193, v193
	v_rcp_f32_e32 v186, v186
	v_rcp_f32_e32 v187, v187
	v_rcp_f32_e32 v188, v188
	v_rcp_f32_e32 v189, v189
	v_rcp_f32_e32 v182, v182
	v_rcp_f32_e32 v183, v183
	v_rcp_f32_e32 v184, v184
	v_rcp_f32_e32 v185, v185
	v_rcp_f32_e32 v158, v158
	v_rcp_f32_e32 v159, v159
	v_rcp_f32_e32 v160, v160
	v_rcp_f32_e32 v161, v161
	s_nop 1
	v_pk_mul_f32 v[114:115], v[114:115], v[190:191]
	v_pk_mul_f32 v[98:99], v[98:99], v[190:191]
	v_pk_mul_f32 v[82:83], v[82:83], v[190:191]
	v_pk_mul_f32 v[66:67], v[66:67], v[190:191]
	v_pk_mul_f32 v[50:51], v[50:51], v[190:191]
	v_pk_mul_f32 v[34:35], v[34:35], v[190:191]
	v_pk_mul_f32 v[18:19], v[18:19], v[190:191]
	v_pk_mul_f32 v[2:3], v[2:3], v[190:191]
	v_pk_mul_f32 v[116:117], v[116:117], v[192:193]
	v_pk_mul_f32 v[100:101], v[100:101], v[192:193]
	v_pk_mul_f32 v[84:85], v[84:85], v[192:193]
	v_pk_mul_f32 v[68:69], v[68:69], v[192:193]
	v_pk_mul_f32 v[52:53], v[52:53], v[192:193]
	v_pk_mul_f32 v[36:37], v[36:37], v[192:193]
	v_pk_mul_f32 v[20:21], v[20:21], v[192:193]
	v_pk_mul_f32 v[4:5], v[4:5], v[192:193]
	v_pk_mul_f32 v[118:119], v[118:119], v[186:187]
	v_pk_mul_f32 v[102:103], v[102:103], v[186:187]
	v_pk_mul_f32 v[86:87], v[86:87], v[186:187]
	v_pk_mul_f32 v[70:71], v[70:71], v[186:187]
	v_pk_mul_f32 v[54:55], v[54:55], v[186:187]
	v_pk_mul_f32 v[38:39], v[38:39], v[186:187]
	v_pk_mul_f32 v[22:23], v[22:23], v[186:187]
	v_pk_mul_f32 v[6:7], v[6:7], v[186:187]
	v_pk_mul_f32 v[120:121], v[120:121], v[188:189]
	v_pk_mul_f32 v[104:105], v[104:105], v[188:189]
	v_pk_mul_f32 v[88:89], v[88:89], v[188:189]
	v_pk_mul_f32 v[72:73], v[72:73], v[188:189]
	v_pk_mul_f32 v[56:57], v[56:57], v[188:189]
	v_pk_mul_f32 v[40:41], v[40:41], v[188:189]
	v_pk_mul_f32 v[24:25], v[24:25], v[188:189]
	v_pk_mul_f32 v[8:9], v[8:9], v[188:189]
	v_pk_mul_f32 v[122:123], v[122:123], v[182:183]
	v_pk_mul_f32 v[106:107], v[106:107], v[182:183]
	v_pk_mul_f32 v[90:91], v[90:91], v[182:183]
	v_pk_mul_f32 v[74:75], v[74:75], v[182:183]
	v_pk_mul_f32 v[58:59], v[58:59], v[182:183]
	v_pk_mul_f32 v[42:43], v[42:43], v[182:183]
	v_pk_mul_f32 v[26:27], v[26:27], v[182:183]
	v_pk_mul_f32 v[10:11], v[10:11], v[182:183]
	v_pk_mul_f32 v[124:125], v[124:125], v[184:185]
	v_pk_mul_f32 v[108:109], v[108:109], v[184:185]
	v_pk_mul_f32 v[92:93], v[92:93], v[184:185]
	v_pk_mul_f32 v[76:77], v[76:77], v[184:185]
	v_pk_mul_f32 v[60:61], v[60:61], v[184:185]
	v_pk_mul_f32 v[44:45], v[44:45], v[184:185]
	v_pk_mul_f32 v[28:29], v[28:29], v[184:185]
	v_pk_mul_f32 v[12:13], v[12:13], v[184:185]
	v_pk_mul_f32 v[126:127], v[126:127], v[158:159]
	v_pk_mul_f32 v[110:111], v[110:111], v[158:159]
	v_pk_mul_f32 v[94:95], v[94:95], v[158:159]
	v_pk_mul_f32 v[78:79], v[78:79], v[158:159]
	v_pk_mul_f32 v[62:63], v[62:63], v[158:159]
	v_pk_mul_f32 v[46:47], v[46:47], v[158:159]
	v_pk_mul_f32 v[30:31], v[30:31], v[158:159]
	v_pk_mul_f32 v[14:15], v[14:15], v[158:159]
	v_pk_mul_f32 v[128:129], v[128:129], v[160:161]
	v_pk_mul_f32 v[112:113], v[112:113], v[160:161]
	v_pk_mul_f32 v[96:97], v[96:97], v[160:161]
	v_pk_mul_f32 v[80:81], v[80:81], v[160:161]
	v_pk_mul_f32 v[64:65], v[64:65], v[160:161]
	v_pk_mul_f32 v[48:49], v[48:49], v[160:161]
	v_pk_mul_f32 v[32:33], v[32:33], v[160:161]
	v_pk_mul_f32 v[16:17], v[16:17], v[160:161]
	v_mov_b32_dpp v0, v114 quad_perm:[1,0,3,2] row_mask:0xf bank_mask:0xf bound_ctrl:1
	v_mov_b32_dpp v190, v98 quad_perm:[1,0,3,2] row_mask:0xf bank_mask:0xf bound_ctrl:1
	v_mov_b32_dpp v191, v82 quad_perm:[1,0,3,2] row_mask:0xf bank_mask:0xf bound_ctrl:1
	v_mov_b32_dpp v192, v66 quad_perm:[1,0,3,2] row_mask:0xf bank_mask:0xf bound_ctrl:1
	v_cvt_pk_bf16_f32 v114, v114, v0
	v_cvt_pk_bf16_f32 v98, v98, v190
	v_cvt_pk_bf16_f32 v82, v82, v191
	v_cvt_pk_bf16_f32 v66, v66, v192
	v_mov_b32_dpp v0, v50 quad_perm:[1,0,3,2] row_mask:0xf bank_mask:0xf bound_ctrl:1
	v_mov_b32_dpp v190, v34 quad_perm:[1,0,3,2] row_mask:0xf bank_mask:0xf bound_ctrl:1
	v_mov_b32_dpp v191, v18 quad_perm:[1,0,3,2] row_mask:0xf bank_mask:0xf bound_ctrl:1
	v_mov_b32_dpp v192, v2 quad_perm:[1,0,3,2] row_mask:0xf bank_mask:0xf bound_ctrl:1
	v_cvt_pk_bf16_f32 v50, v50, v0
	v_cvt_pk_bf16_f32 v34, v34, v190
	v_cvt_pk_bf16_f32 v18, v18, v191
	v_cvt_pk_bf16_f32 v2, v2, v192
	v_mov_b32_dpp v0, v115 quad_perm:[1,0,3,2] row_mask:0xf bank_mask:0xf bound_ctrl:1
	v_mov_b32_dpp v190, v99 quad_perm:[1,0,3,2] row_mask:0xf bank_mask:0xf bound_ctrl:1
	v_mov_b32_dpp v191, v83 quad_perm:[1,0,3,2] row_mask:0xf bank_mask:0xf bound_ctrl:1
	v_mov_b32_dpp v192, v67 quad_perm:[1,0,3,2] row_mask:0xf bank_mask:0xf bound_ctrl:1
	v_cvt_pk_bf16_f32 v115, v115, v0
	v_cvt_pk_bf16_f32 v99, v99, v190
	v_cvt_pk_bf16_f32 v83, v83, v191
	v_cvt_pk_bf16_f32 v67, v67, v192
	v_mov_b32_dpp v0, v51 quad_perm:[1,0,3,2] row_mask:0xf bank_mask:0xf bound_ctrl:1
	v_mov_b32_dpp v190, v35 quad_perm:[1,0,3,2] row_mask:0xf bank_mask:0xf bound_ctrl:1
	v_mov_b32_dpp v191, v19 quad_perm:[1,0,3,2] row_mask:0xf bank_mask:0xf bound_ctrl:1
	v_mov_b32_dpp v192, v3 quad_perm:[1,0,3,2] row_mask:0xf bank_mask:0xf bound_ctrl:1
	v_cvt_pk_bf16_f32 v51, v51, v0
	v_cvt_pk_bf16_f32 v35, v35, v190
	v_cvt_pk_bf16_f32 v19, v19, v191
	v_cvt_pk_bf16_f32 v3, v3, v192
	v_mov_b32_dpp v0, v116 quad_perm:[1,0,3,2] row_mask:0xf bank_mask:0xf bound_ctrl:1
	v_mov_b32_dpp v190, v100 quad_perm:[1,0,3,2] row_mask:0xf bank_mask:0xf bound_ctrl:1
	v_mov_b32_dpp v191, v84 quad_perm:[1,0,3,2] row_mask:0xf bank_mask:0xf bound_ctrl:1
	v_mov_b32_dpp v192, v68 quad_perm:[1,0,3,2] row_mask:0xf bank_mask:0xf bound_ctrl:1
	v_cvt_pk_bf16_f32 v116, v116, v0
	v_cvt_pk_bf16_f32 v100, v100, v190
	v_cvt_pk_bf16_f32 v84, v84, v191
	v_cvt_pk_bf16_f32 v68, v68, v192
	v_mov_b32_dpp v0, v52 quad_perm:[1,0,3,2] row_mask:0xf bank_mask:0xf bound_ctrl:1
	v_mov_b32_dpp v190, v36 quad_perm:[1,0,3,2] row_mask:0xf bank_mask:0xf bound_ctrl:1
	v_mov_b32_dpp v191, v20 quad_perm:[1,0,3,2] row_mask:0xf bank_mask:0xf bound_ctrl:1
	v_mov_b32_dpp v192, v4 quad_perm:[1,0,3,2] row_mask:0xf bank_mask:0xf bound_ctrl:1
	v_cvt_pk_bf16_f32 v52, v52, v0
	v_cvt_pk_bf16_f32 v36, v36, v190
	v_cvt_pk_bf16_f32 v20, v20, v191
	v_cvt_pk_bf16_f32 v4, v4, v192
	v_mov_b32_dpp v0, v117 quad_perm:[1,0,3,2] row_mask:0xf bank_mask:0xf bound_ctrl:1
	v_mov_b32_dpp v190, v101 quad_perm:[1,0,3,2] row_mask:0xf bank_mask:0xf bound_ctrl:1
	v_mov_b32_dpp v191, v85 quad_perm:[1,0,3,2] row_mask:0xf bank_mask:0xf bound_ctrl:1
	v_mov_b32_dpp v192, v69 quad_perm:[1,0,3,2] row_mask:0xf bank_mask:0xf bound_ctrl:1
	v_cvt_pk_bf16_f32 v117, v117, v0
	v_cvt_pk_bf16_f32 v101, v101, v190
	v_cvt_pk_bf16_f32 v85, v85, v191
	v_cvt_pk_bf16_f32 v69, v69, v192
	v_mov_b32_dpp v0, v53 quad_perm:[1,0,3,2] row_mask:0xf bank_mask:0xf bound_ctrl:1
	v_mov_b32_dpp v190, v37 quad_perm:[1,0,3,2] row_mask:0xf bank_mask:0xf bound_ctrl:1
	v_mov_b32_dpp v191, v21 quad_perm:[1,0,3,2] row_mask:0xf bank_mask:0xf bound_ctrl:1
	v_mov_b32_dpp v192, v5 quad_perm:[1,0,3,2] row_mask:0xf bank_mask:0xf bound_ctrl:1
	v_cvt_pk_bf16_f32 v53, v53, v0
	v_cvt_pk_bf16_f32 v37, v37, v190
	v_cvt_pk_bf16_f32 v21, v21, v191
	v_cvt_pk_bf16_f32 v5, v5, v192
	v_mov_b32_dpp v0, v118 quad_perm:[1,0,3,2] row_mask:0xf bank_mask:0xf bound_ctrl:1
	v_mov_b32_dpp v190, v102 quad_perm:[1,0,3,2] row_mask:0xf bank_mask:0xf bound_ctrl:1
	v_mov_b32_dpp v191, v86 quad_perm:[1,0,3,2] row_mask:0xf bank_mask:0xf bound_ctrl:1
	v_mov_b32_dpp v192, v70 quad_perm:[1,0,3,2] row_mask:0xf bank_mask:0xf bound_ctrl:1
	v_cvt_pk_bf16_f32 v118, v118, v0
	v_cvt_pk_bf16_f32 v102, v102, v190
	v_cvt_pk_bf16_f32 v86, v86, v191
	v_cvt_pk_bf16_f32 v70, v70, v192
	v_mov_b32_dpp v0, v54 quad_perm:[1,0,3,2] row_mask:0xf bank_mask:0xf bound_ctrl:1
	v_mov_b32_dpp v190, v38 quad_perm:[1,0,3,2] row_mask:0xf bank_mask:0xf bound_ctrl:1
	v_mov_b32_dpp v191, v22 quad_perm:[1,0,3,2] row_mask:0xf bank_mask:0xf bound_ctrl:1
	v_mov_b32_dpp v192, v6 quad_perm:[1,0,3,2] row_mask:0xf bank_mask:0xf bound_ctrl:1
	v_cvt_pk_bf16_f32 v54, v54, v0
	v_cvt_pk_bf16_f32 v38, v38, v190
	v_cvt_pk_bf16_f32 v22, v22, v191
	v_cvt_pk_bf16_f32 v6, v6, v192
	v_mov_b32_dpp v0, v119 quad_perm:[1,0,3,2] row_mask:0xf bank_mask:0xf bound_ctrl:1
	v_mov_b32_dpp v190, v103 quad_perm:[1,0,3,2] row_mask:0xf bank_mask:0xf bound_ctrl:1
	v_mov_b32_dpp v191, v87 quad_perm:[1,0,3,2] row_mask:0xf bank_mask:0xf bound_ctrl:1
	v_mov_b32_dpp v192, v71 quad_perm:[1,0,3,2] row_mask:0xf bank_mask:0xf bound_ctrl:1
	v_cvt_pk_bf16_f32 v119, v119, v0
	v_cvt_pk_bf16_f32 v103, v103, v190
	v_cvt_pk_bf16_f32 v87, v87, v191
	v_cvt_pk_bf16_f32 v71, v71, v192
	v_mov_b32_dpp v0, v55 quad_perm:[1,0,3,2] row_mask:0xf bank_mask:0xf bound_ctrl:1
	v_mov_b32_dpp v190, v39 quad_perm:[1,0,3,2] row_mask:0xf bank_mask:0xf bound_ctrl:1
	v_mov_b32_dpp v191, v23 quad_perm:[1,0,3,2] row_mask:0xf bank_mask:0xf bound_ctrl:1
	v_mov_b32_dpp v192, v7 quad_perm:[1,0,3,2] row_mask:0xf bank_mask:0xf bound_ctrl:1
	v_cvt_pk_bf16_f32 v55, v55, v0
	v_cvt_pk_bf16_f32 v39, v39, v190
	v_cvt_pk_bf16_f32 v23, v23, v191
	v_cvt_pk_bf16_f32 v7, v7, v192
	v_mov_b32_dpp v0, v120 quad_perm:[1,0,3,2] row_mask:0xf bank_mask:0xf bound_ctrl:1
	v_mov_b32_dpp v190, v104 quad_perm:[1,0,3,2] row_mask:0xf bank_mask:0xf bound_ctrl:1
	v_mov_b32_dpp v191, v88 quad_perm:[1,0,3,2] row_mask:0xf bank_mask:0xf bound_ctrl:1
	v_mov_b32_dpp v192, v72 quad_perm:[1,0,3,2] row_mask:0xf bank_mask:0xf bound_ctrl:1
	v_cvt_pk_bf16_f32 v120, v120, v0
	v_cvt_pk_bf16_f32 v104, v104, v190
	v_cvt_pk_bf16_f32 v88, v88, v191
	v_cvt_pk_bf16_f32 v72, v72, v192
	v_mov_b32_dpp v0, v56 quad_perm:[1,0,3,2] row_mask:0xf bank_mask:0xf bound_ctrl:1
	v_mov_b32_dpp v190, v40 quad_perm:[1,0,3,2] row_mask:0xf bank_mask:0xf bound_ctrl:1
	v_mov_b32_dpp v191, v24 quad_perm:[1,0,3,2] row_mask:0xf bank_mask:0xf bound_ctrl:1
	v_mov_b32_dpp v192, v8 quad_perm:[1,0,3,2] row_mask:0xf bank_mask:0xf bound_ctrl:1
	v_cvt_pk_bf16_f32 v56, v56, v0
	v_cvt_pk_bf16_f32 v40, v40, v190
	v_cvt_pk_bf16_f32 v24, v24, v191
	v_cvt_pk_bf16_f32 v8, v8, v192
	v_mov_b32_dpp v0, v121 quad_perm:[1,0,3,2] row_mask:0xf bank_mask:0xf bound_ctrl:1
	v_mov_b32_dpp v190, v105 quad_perm:[1,0,3,2] row_mask:0xf bank_mask:0xf bound_ctrl:1
	v_mov_b32_dpp v191, v89 quad_perm:[1,0,3,2] row_mask:0xf bank_mask:0xf bound_ctrl:1
	v_mov_b32_dpp v192, v73 quad_perm:[1,0,3,2] row_mask:0xf bank_mask:0xf bound_ctrl:1
	v_cvt_pk_bf16_f32 v121, v121, v0
	v_cvt_pk_bf16_f32 v105, v105, v190
	v_cvt_pk_bf16_f32 v89, v89, v191
	v_cvt_pk_bf16_f32 v73, v73, v192
	v_mov_b32_dpp v0, v57 quad_perm:[1,0,3,2] row_mask:0xf bank_mask:0xf bound_ctrl:1
	v_mov_b32_dpp v190, v41 quad_perm:[1,0,3,2] row_mask:0xf bank_mask:0xf bound_ctrl:1
	v_mov_b32_dpp v191, v25 quad_perm:[1,0,3,2] row_mask:0xf bank_mask:0xf bound_ctrl:1
	v_mov_b32_dpp v192, v9 quad_perm:[1,0,3,2] row_mask:0xf bank_mask:0xf bound_ctrl:1
	v_cvt_pk_bf16_f32 v57, v57, v0
	v_cvt_pk_bf16_f32 v41, v41, v190
	v_cvt_pk_bf16_f32 v25, v25, v191
	v_cvt_pk_bf16_f32 v9, v9, v192
	v_mov_b32_dpp v0, v122 quad_perm:[1,0,3,2] row_mask:0xf bank_mask:0xf bound_ctrl:1
	v_mov_b32_dpp v190, v106 quad_perm:[1,0,3,2] row_mask:0xf bank_mask:0xf bound_ctrl:1
	v_mov_b32_dpp v191, v90 quad_perm:[1,0,3,2] row_mask:0xf bank_mask:0xf bound_ctrl:1
	v_mov_b32_dpp v192, v74 quad_perm:[1,0,3,2] row_mask:0xf bank_mask:0xf bound_ctrl:1
	v_cvt_pk_bf16_f32 v122, v122, v0
	v_cvt_pk_bf16_f32 v106, v106, v190
	v_cvt_pk_bf16_f32 v90, v90, v191
	v_cvt_pk_bf16_f32 v74, v74, v192
	v_mov_b32_dpp v0, v58 quad_perm:[1,0,3,2] row_mask:0xf bank_mask:0xf bound_ctrl:1
	v_mov_b32_dpp v190, v42 quad_perm:[1,0,3,2] row_mask:0xf bank_mask:0xf bound_ctrl:1
	v_mov_b32_dpp v191, v26 quad_perm:[1,0,3,2] row_mask:0xf bank_mask:0xf bound_ctrl:1
	v_mov_b32_dpp v192, v10 quad_perm:[1,0,3,2] row_mask:0xf bank_mask:0xf bound_ctrl:1
	v_cvt_pk_bf16_f32 v58, v58, v0
	v_cvt_pk_bf16_f32 v42, v42, v190
	v_cvt_pk_bf16_f32 v26, v26, v191
	v_cvt_pk_bf16_f32 v10, v10, v192
	v_mov_b32_dpp v0, v123 quad_perm:[1,0,3,2] row_mask:0xf bank_mask:0xf bound_ctrl:1
	v_mov_b32_dpp v190, v107 quad_perm:[1,0,3,2] row_mask:0xf bank_mask:0xf bound_ctrl:1
	v_mov_b32_dpp v191, v91 quad_perm:[1,0,3,2] row_mask:0xf bank_mask:0xf bound_ctrl:1
	v_mov_b32_dpp v192, v75 quad_perm:[1,0,3,2] row_mask:0xf bank_mask:0xf bound_ctrl:1
	v_cvt_pk_bf16_f32 v123, v123, v0
	v_cvt_pk_bf16_f32 v107, v107, v190
	v_cvt_pk_bf16_f32 v91, v91, v191
	v_cvt_pk_bf16_f32 v75, v75, v192
	v_mov_b32_dpp v0, v59 quad_perm:[1,0,3,2] row_mask:0xf bank_mask:0xf bound_ctrl:1
	v_mov_b32_dpp v190, v43 quad_perm:[1,0,3,2] row_mask:0xf bank_mask:0xf bound_ctrl:1
	v_mov_b32_dpp v191, v27 quad_perm:[1,0,3,2] row_mask:0xf bank_mask:0xf bound_ctrl:1
	v_mov_b32_dpp v192, v11 quad_perm:[1,0,3,2] row_mask:0xf bank_mask:0xf bound_ctrl:1
	v_cvt_pk_bf16_f32 v59, v59, v0
	v_cvt_pk_bf16_f32 v43, v43, v190
	v_cvt_pk_bf16_f32 v27, v27, v191
	v_cvt_pk_bf16_f32 v11, v11, v192
	v_mov_b32_dpp v0, v124 quad_perm:[1,0,3,2] row_mask:0xf bank_mask:0xf bound_ctrl:1
	v_mov_b32_dpp v190, v108 quad_perm:[1,0,3,2] row_mask:0xf bank_mask:0xf bound_ctrl:1
	v_mov_b32_dpp v191, v92 quad_perm:[1,0,3,2] row_mask:0xf bank_mask:0xf bound_ctrl:1
	v_mov_b32_dpp v192, v76 quad_perm:[1,0,3,2] row_mask:0xf bank_mask:0xf bound_ctrl:1
	v_cvt_pk_bf16_f32 v124, v124, v0
	v_cvt_pk_bf16_f32 v108, v108, v190
	v_cvt_pk_bf16_f32 v92, v92, v191
	v_cvt_pk_bf16_f32 v76, v76, v192
	v_mov_b32_dpp v0, v60 quad_perm:[1,0,3,2] row_mask:0xf bank_mask:0xf bound_ctrl:1
	v_mov_b32_dpp v190, v44 quad_perm:[1,0,3,2] row_mask:0xf bank_mask:0xf bound_ctrl:1
	v_mov_b32_dpp v191, v28 quad_perm:[1,0,3,2] row_mask:0xf bank_mask:0xf bound_ctrl:1
	v_mov_b32_dpp v192, v12 quad_perm:[1,0,3,2] row_mask:0xf bank_mask:0xf bound_ctrl:1
	v_cvt_pk_bf16_f32 v60, v60, v0
	v_cvt_pk_bf16_f32 v44, v44, v190
	v_cvt_pk_bf16_f32 v28, v28, v191
	v_cvt_pk_bf16_f32 v12, v12, v192
	v_mov_b32_dpp v0, v125 quad_perm:[1,0,3,2] row_mask:0xf bank_mask:0xf bound_ctrl:1
	v_mov_b32_dpp v190, v109 quad_perm:[1,0,3,2] row_mask:0xf bank_mask:0xf bound_ctrl:1
	v_mov_b32_dpp v191, v93 quad_perm:[1,0,3,2] row_mask:0xf bank_mask:0xf bound_ctrl:1
	v_mov_b32_dpp v192, v77 quad_perm:[1,0,3,2] row_mask:0xf bank_mask:0xf bound_ctrl:1
	v_cvt_pk_bf16_f32 v125, v125, v0
	v_cvt_pk_bf16_f32 v109, v109, v190
	v_cvt_pk_bf16_f32 v93, v93, v191
	v_cvt_pk_bf16_f32 v77, v77, v192
	v_mov_b32_dpp v0, v61 quad_perm:[1,0,3,2] row_mask:0xf bank_mask:0xf bound_ctrl:1
	v_mov_b32_dpp v190, v45 quad_perm:[1,0,3,2] row_mask:0xf bank_mask:0xf bound_ctrl:1
	v_mov_b32_dpp v191, v29 quad_perm:[1,0,3,2] row_mask:0xf bank_mask:0xf bound_ctrl:1
	v_mov_b32_dpp v192, v13 quad_perm:[1,0,3,2] row_mask:0xf bank_mask:0xf bound_ctrl:1
	v_cvt_pk_bf16_f32 v61, v61, v0
	v_cvt_pk_bf16_f32 v45, v45, v190
	v_cvt_pk_bf16_f32 v29, v29, v191
	v_cvt_pk_bf16_f32 v13, v13, v192
	v_mov_b32_dpp v0, v126 quad_perm:[1,0,3,2] row_mask:0xf bank_mask:0xf bound_ctrl:1
	v_mov_b32_dpp v190, v110 quad_perm:[1,0,3,2] row_mask:0xf bank_mask:0xf bound_ctrl:1
	v_mov_b32_dpp v191, v94 quad_perm:[1,0,3,2] row_mask:0xf bank_mask:0xf bound_ctrl:1
	v_mov_b32_dpp v192, v78 quad_perm:[1,0,3,2] row_mask:0xf bank_mask:0xf bound_ctrl:1
	v_cvt_pk_bf16_f32 v126, v126, v0
	v_cvt_pk_bf16_f32 v110, v110, v190
	v_cvt_pk_bf16_f32 v94, v94, v191
	v_cvt_pk_bf16_f32 v78, v78, v192
	v_mov_b32_dpp v0, v62 quad_perm:[1,0,3,2] row_mask:0xf bank_mask:0xf bound_ctrl:1
	v_mov_b32_dpp v190, v46 quad_perm:[1,0,3,2] row_mask:0xf bank_mask:0xf bound_ctrl:1
	v_mov_b32_dpp v191, v30 quad_perm:[1,0,3,2] row_mask:0xf bank_mask:0xf bound_ctrl:1
	v_mov_b32_dpp v192, v14 quad_perm:[1,0,3,2] row_mask:0xf bank_mask:0xf bound_ctrl:1
	v_cvt_pk_bf16_f32 v62, v62, v0
	v_cvt_pk_bf16_f32 v46, v46, v190
	v_cvt_pk_bf16_f32 v30, v30, v191
	v_cvt_pk_bf16_f32 v14, v14, v192
	v_mov_b32_dpp v0, v127 quad_perm:[1,0,3,2] row_mask:0xf bank_mask:0xf bound_ctrl:1
	v_mov_b32_dpp v190, v111 quad_perm:[1,0,3,2] row_mask:0xf bank_mask:0xf bound_ctrl:1
	v_mov_b32_dpp v191, v95 quad_perm:[1,0,3,2] row_mask:0xf bank_mask:0xf bound_ctrl:1
	v_mov_b32_dpp v192, v79 quad_perm:[1,0,3,2] row_mask:0xf bank_mask:0xf bound_ctrl:1
	v_cvt_pk_bf16_f32 v127, v127, v0
	v_cvt_pk_bf16_f32 v111, v111, v190
	v_cvt_pk_bf16_f32 v95, v95, v191
	v_cvt_pk_bf16_f32 v79, v79, v192
	v_mov_b32_dpp v0, v63 quad_perm:[1,0,3,2] row_mask:0xf bank_mask:0xf bound_ctrl:1
	v_mov_b32_dpp v190, v47 quad_perm:[1,0,3,2] row_mask:0xf bank_mask:0xf bound_ctrl:1
	v_mov_b32_dpp v191, v31 quad_perm:[1,0,3,2] row_mask:0xf bank_mask:0xf bound_ctrl:1
	v_mov_b32_dpp v192, v15 quad_perm:[1,0,3,2] row_mask:0xf bank_mask:0xf bound_ctrl:1
	v_cvt_pk_bf16_f32 v63, v63, v0
	v_cvt_pk_bf16_f32 v47, v47, v190
	v_cvt_pk_bf16_f32 v31, v31, v191
	v_cvt_pk_bf16_f32 v15, v15, v192
	v_mov_b32_dpp v0, v128 quad_perm:[1,0,3,2] row_mask:0xf bank_mask:0xf bound_ctrl:1
	v_mov_b32_dpp v190, v112 quad_perm:[1,0,3,2] row_mask:0xf bank_mask:0xf bound_ctrl:1
	v_mov_b32_dpp v191, v96 quad_perm:[1,0,3,2] row_mask:0xf bank_mask:0xf bound_ctrl:1
	v_mov_b32_dpp v192, v80 quad_perm:[1,0,3,2] row_mask:0xf bank_mask:0xf bound_ctrl:1
	v_cvt_pk_bf16_f32 v128, v128, v0
	v_cvt_pk_bf16_f32 v112, v112, v190
	v_cvt_pk_bf16_f32 v96, v96, v191
	v_cvt_pk_bf16_f32 v80, v80, v192
	v_mov_b32_dpp v0, v64 quad_perm:[1,0,3,2] row_mask:0xf bank_mask:0xf bound_ctrl:1
	v_mov_b32_dpp v190, v48 quad_perm:[1,0,3,2] row_mask:0xf bank_mask:0xf bound_ctrl:1
	v_mov_b32_dpp v191, v32 quad_perm:[1,0,3,2] row_mask:0xf bank_mask:0xf bound_ctrl:1
	v_mov_b32_dpp v192, v16 quad_perm:[1,0,3,2] row_mask:0xf bank_mask:0xf bound_ctrl:1
	v_cvt_pk_bf16_f32 v64, v64, v0
	v_cvt_pk_bf16_f32 v48, v48, v190
	v_cvt_pk_bf16_f32 v32, v32, v191
	v_cvt_pk_bf16_f32 v16, v16, v192
	v_mov_b32_dpp v0, v129 quad_perm:[1,0,3,2] row_mask:0xf bank_mask:0xf bound_ctrl:1
	v_mov_b32_dpp v190, v113 quad_perm:[1,0,3,2] row_mask:0xf bank_mask:0xf bound_ctrl:1
	v_mov_b32_dpp v191, v97 quad_perm:[1,0,3,2] row_mask:0xf bank_mask:0xf bound_ctrl:1
	v_mov_b32_dpp v192, v81 quad_perm:[1,0,3,2] row_mask:0xf bank_mask:0xf bound_ctrl:1
	v_cvt_pk_bf16_f32 v129, v129, v0
	v_cvt_pk_bf16_f32 v113, v113, v190
	v_cvt_pk_bf16_f32 v97, v97, v191
	v_cvt_pk_bf16_f32 v81, v81, v192
	v_mov_b32_dpp v0, v65 quad_perm:[1,0,3,2] row_mask:0xf bank_mask:0xf bound_ctrl:1
	v_mov_b32_dpp v190, v49 quad_perm:[1,0,3,2] row_mask:0xf bank_mask:0xf bound_ctrl:1
	v_mov_b32_dpp v191, v33 quad_perm:[1,0,3,2] row_mask:0xf bank_mask:0xf bound_ctrl:1
	v_mov_b32_dpp v192, v17 quad_perm:[1,0,3,2] row_mask:0xf bank_mask:0xf bound_ctrl:1
	v_cvt_pk_bf16_f32 v65, v65, v0
	v_cvt_pk_bf16_f32 v49, v49, v190
	v_cvt_pk_bf16_f32 v33, v33, v191
	v_cvt_pk_bf16_f32 v17, v17, v192
	s_mov_b64 exec, s[0:1]
	global_store_dword v[194:195], v114, off
	global_store_dword v[194:195], v98, off offset:64
	global_store_dword v[194:195], v82, off offset:128
	global_store_dword v[194:195], v66, off offset:192
	global_store_dword v[194:195], v50, off offset:256
	global_store_dword v[194:195], v34, off offset:320
	global_store_dword v[194:195], v18, off offset:384
	global_store_dword v[194:195], v2, off offset:448
	s_mov_b64 s[2:3], 0x2000
	v_lshl_add_u64 v[190:191], v[194:195], 0, s[2:3]
	global_store_dword v[190:191], v115, off
	global_store_dword v[190:191], v99, off offset:64
	global_store_dword v[190:191], v83, off offset:128
	global_store_dword v[190:191], v67, off offset:192
	global_store_dword v[190:191], v51, off offset:256
	global_store_dword v[190:191], v35, off offset:320
	global_store_dword v[190:191], v19, off offset:384
	global_store_dword v[190:191], v3, off offset:448
	s_mov_b64 s[2:3], 0x4000
	v_lshl_add_u64 v[192:193], v[194:195], 0, s[2:3]
	global_store_dword v[192:193], v116, off
	global_store_dword v[192:193], v100, off offset:64
	global_store_dword v[192:193], v84, off offset:128
	global_store_dword v[192:193], v68, off offset:192
	global_store_dword v[192:193], v52, off offset:256
	global_store_dword v[192:193], v36, off offset:320
	global_store_dword v[192:193], v20, off offset:384
	global_store_dword v[192:193], v4, off offset:448
	s_mov_b64 s[2:3], 0x6000
	v_lshl_add_u64 v[190:191], v[194:195], 0, s[2:3]
	global_store_dword v[190:191], v117, off
	global_store_dword v[190:191], v101, off offset:64
	global_store_dword v[190:191], v85, off offset:128
	global_store_dword v[190:191], v69, off offset:192
	global_store_dword v[190:191], v53, off offset:256
	global_store_dword v[190:191], v37, off offset:320
	global_store_dword v[190:191], v21, off offset:384
	global_store_dword v[190:191], v5, off offset:448
	s_mov_b64 s[2:3], 0x10000
	v_lshl_add_u64 v[192:193], v[194:195], 0, s[2:3]
	global_store_dword v[192:193], v118, off
	global_store_dword v[192:193], v102, off offset:64
	global_store_dword v[192:193], v86, off offset:128
	global_store_dword v[192:193], v70, off offset:192
	global_store_dword v[192:193], v54, off offset:256
	global_store_dword v[192:193], v38, off offset:320
	global_store_dword v[192:193], v22, off offset:384
	global_store_dword v[192:193], v6, off offset:448
	s_mov_b64 s[2:3], 0x12000
	v_lshl_add_u64 v[190:191], v[194:195], 0, s[2:3]
	global_store_dword v[190:191], v119, off
	global_store_dword v[190:191], v103, off offset:64
	global_store_dword v[190:191], v87, off offset:128
	global_store_dword v[190:191], v71, off offset:192
	global_store_dword v[190:191], v55, off offset:256
	global_store_dword v[190:191], v39, off offset:320
	global_store_dword v[190:191], v23, off offset:384
	global_store_dword v[190:191], v7, off offset:448
	s_mov_b64 s[2:3], 0x14000
	v_lshl_add_u64 v[192:193], v[194:195], 0, s[2:3]
	global_store_dword v[192:193], v120, off
	global_store_dword v[192:193], v104, off offset:64
	global_store_dword v[192:193], v88, off offset:128
	global_store_dword v[192:193], v72, off offset:192
	global_store_dword v[192:193], v56, off offset:256
	global_store_dword v[192:193], v40, off offset:320
	global_store_dword v[192:193], v24, off offset:384
	global_store_dword v[192:193], v8, off offset:448
	s_mov_b64 s[2:3], 0x16000
	v_lshl_add_u64 v[190:191], v[194:195], 0, s[2:3]
	global_store_dword v[190:191], v121, off
	global_store_dword v[190:191], v105, off offset:64
	global_store_dword v[190:191], v89, off offset:128
	global_store_dword v[190:191], v73, off offset:192
	global_store_dword v[190:191], v57, off offset:256
	global_store_dword v[190:191], v41, off offset:320
	global_store_dword v[190:191], v25, off offset:384
	global_store_dword v[190:191], v9, off offset:448
	s_mov_b64 s[2:3], 0x20000
	v_lshl_add_u64 v[192:193], v[194:195], 0, s[2:3]
	global_store_dword v[192:193], v122, off
	global_store_dword v[192:193], v106, off offset:64
	global_store_dword v[192:193], v90, off offset:128
	global_store_dword v[192:193], v74, off offset:192
	global_store_dword v[192:193], v58, off offset:256
	global_store_dword v[192:193], v42, off offset:320
	global_store_dword v[192:193], v26, off offset:384
	global_store_dword v[192:193], v10, off offset:448
	s_mov_b64 s[2:3], 0x22000
	v_lshl_add_u64 v[190:191], v[194:195], 0, s[2:3]
	global_store_dword v[190:191], v123, off
	global_store_dword v[190:191], v107, off offset:64
	global_store_dword v[190:191], v91, off offset:128
	global_store_dword v[190:191], v75, off offset:192
	global_store_dword v[190:191], v59, off offset:256
	global_store_dword v[190:191], v43, off offset:320
	global_store_dword v[190:191], v27, off offset:384
	global_store_dword v[190:191], v11, off offset:448
	s_mov_b64 s[2:3], 0x24000
	v_lshl_add_u64 v[192:193], v[194:195], 0, s[2:3]
	global_store_dword v[192:193], v124, off
	global_store_dword v[192:193], v108, off offset:64
	global_store_dword v[192:193], v92, off offset:128
	global_store_dword v[192:193], v76, off offset:192
	global_store_dword v[192:193], v60, off offset:256
	global_store_dword v[192:193], v44, off offset:320
	global_store_dword v[192:193], v28, off offset:384
	global_store_dword v[192:193], v12, off offset:448
	s_mov_b64 s[2:3], 0x26000
	v_lshl_add_u64 v[190:191], v[194:195], 0, s[2:3]
	global_store_dword v[190:191], v125, off
	global_store_dword v[190:191], v109, off offset:64
	global_store_dword v[190:191], v93, off offset:128
	global_store_dword v[190:191], v77, off offset:192
	global_store_dword v[190:191], v61, off offset:256
	global_store_dword v[190:191], v45, off offset:320
	global_store_dword v[190:191], v29, off offset:384
	global_store_dword v[190:191], v13, off offset:448
	s_mov_b64 s[2:3], 0x30000
	v_lshl_add_u64 v[192:193], v[194:195], 0, s[2:3]
	global_store_dword v[192:193], v126, off
	global_store_dword v[192:193], v110, off offset:64
	global_store_dword v[192:193], v94, off offset:128
	global_store_dword v[192:193], v78, off offset:192
	global_store_dword v[192:193], v62, off offset:256
	global_store_dword v[192:193], v46, off offset:320
	global_store_dword v[192:193], v30, off offset:384
	global_store_dword v[192:193], v14, off offset:448
	s_mov_b64 s[2:3], 0x32000
	v_lshl_add_u64 v[190:191], v[194:195], 0, s[2:3]
	global_store_dword v[190:191], v127, off
	global_store_dword v[190:191], v111, off offset:64
	global_store_dword v[190:191], v95, off offset:128
	global_store_dword v[190:191], v79, off offset:192
	global_store_dword v[190:191], v63, off offset:256
	global_store_dword v[190:191], v47, off offset:320
	global_store_dword v[190:191], v31, off offset:384
	global_store_dword v[190:191], v15, off offset:448
	s_mov_b64 s[2:3], 0x34000
	v_lshl_add_u64 v[192:193], v[194:195], 0, s[2:3]
	global_store_dword v[192:193], v128, off
	global_store_dword v[192:193], v112, off offset:64
	global_store_dword v[192:193], v96, off offset:128
	global_store_dword v[192:193], v80, off offset:192
	global_store_dword v[192:193], v64, off offset:256
	global_store_dword v[192:193], v48, off offset:320
	global_store_dword v[192:193], v32, off offset:384
	global_store_dword v[192:193], v16, off offset:448
	s_mov_b64 s[2:3], 0x36000
	v_lshl_add_u64 v[190:191], v[194:195], 0, s[2:3]
	global_store_dword v[190:191], v129, off
	global_store_dword v[190:191], v113, off offset:64
	global_store_dword v[190:191], v97, off offset:128
	global_store_dword v[190:191], v81, off offset:192
	global_store_dword v[190:191], v65, off offset:256
	global_store_dword v[190:191], v49, off offset:320
	global_store_dword v[190:191], v33, off offset:384
	global_store_dword v[190:191], v17, off offset:448
	s_mov_b64 exec, -1
	s_mov_b64 s[2:3], 0
	s_branch .LBB0_1348
